# MoBA own-block epilogue: PML/PO partial-merge loads issued together up front
# baseline (speedup 1.0000x reference)
; __device__ __forceinline__ float xhalf_sum(float v) { auto rr = __builtin_amdgcn_permlane32_swap(__float_as_uint(v), __float_as_uint(v), false, false); return __uint_as_float(rr[0]) + __uint_as_float(rr[1]); }
; template <int DQK, bool MOBA_OWN>
; __device__ __forceinline__ void attn_unit(LAS unsigned char* lds, int b, int h, int qb, const bf16_t* Qp, int ldq, const bf16_t* Kp, int ldk, const bf16_t* Vp, int ldv, bf16_t* Op, int ldo, const bf16_t* PO, const f32x2* PML) {
;     ...
;     float lt = xhalf_sum(l);
;     if (MOBA_OWN) {
;         const int nsel = qb < 3 ? qb : 3;
;         const size_t pidx = ((rowbase + tq) * 8 + h) * 3;
;         float ms[3], ws[3], M = m;
; #pragma unroll
;         for (int sIdx = 0; sIdx < 3; ++sIdx) { ms[sIdx] = -1e30f; ws[sIdx] = 0.f; if (sIdx < nsel) { const f32x2 ml = PML[pidx + sIdx]; ms[sIdx] = ml[0]; ws[sIdx] = ml[1]; M = fmaxf(M, ml[0]); } }
.LBB0_1050:
	v_lshlrev_b64 v[46:47], 3, v[184:185]
	v_readlane_b32 s0, v254, 61
	v_readlane_b32 s8, v254, 59
	s_cmp_lg_u32 s8, 0
	v_or_b32_e32 v46, s0, v46
	v_readlane_b32 s0, v254, 10
	v_readlane_b32 s1, v254, 11
	v_mov_b32_e32 v69, v202
	s_cselect_b64 s[6:7], -1, 0
	v_mad_u64_u32 v[2:3], s[0:1], v46, 24, s[0:1]
	v_permlane32_swap_b32_e32 v202, v69
	v_mad_i32_i24 v3, v47, 24, v3
	v_readlane_b32 s0, v254, 8
	v_readlane_b32 s1, v254, 9
	v_lshlrev_b32_e32 v126, 1, v201
	v_mov_b32_e32 v127, 0
	s_nop 0
	v_lshl_add_u64 v[126:127], s[0:1], 0, v[126:127]
	s_movk_i32 s0, 0x180
	v_mad_u64_u32 v[126:127], vcc, v46, s0, v[126:127]
	v_mov_b32_e32 v128, v127
	v_mad_u64_u32 v[128:129], vcc, v47, s0, v[128:129]
	v_mov_b32_e32 v127, v128
	global_load_dwordx2 v[72:73], v[126:127], off
	global_load_dwordx2 v[74:75], v[126:127], off offset:64
	global_load_dwordx2 v[76:77], v[126:127], off offset:16
	global_load_dwordx2 v[78:79], v[126:127], off offset:80
	global_load_dwordx2 v[80:81], v[126:127], off offset:32
	global_load_dwordx2 v[82:83], v[126:127], off offset:96
	global_load_dwordx2 v[84:85], v[126:127], off offset:48
	global_load_dwordx2 v[86:87], v[126:127], off offset:112
	global_load_dwordx2 v[88:89], v[126:127], off offset:128
	global_load_dwordx2 v[90:91], v[126:127], off offset:192
	global_load_dwordx2 v[92:93], v[126:127], off offset:144
	global_load_dwordx2 v[94:95], v[126:127], off offset:208
	global_load_dwordx2 v[96:97], v[126:127], off offset:160
	global_load_dwordx2 v[98:99], v[126:127], off offset:224
	global_load_dwordx2 v[100:101], v[126:127], off offset:176
	global_load_dwordx2 v[102:103], v[126:127], off offset:240
	global_load_dwordx2 v[104:105], v[126:127], off offset:256
	global_load_dwordx2 v[106:107], v[126:127], off offset:320
	global_load_dwordx2 v[108:109], v[126:127], off offset:272
	global_load_dwordx2 v[110:111], v[126:127], off offset:336
	global_load_dwordx2 v[112:113], v[126:127], off offset:288
	global_load_dwordx2 v[114:115], v[126:127], off offset:352
	global_load_dwordx2 v[116:117], v[126:127], off offset:304
	global_load_dwordx2 v[118:119], v[126:127], off offset:368
	v_mov_b32_e32 v49, 0
	v_mov_b32_e32 v48, 0xf149f2ca
	s_and_b64 vcc, exec, s[6:7]
	v_mov_b32_e32 v66, 0xf149f2ca
	v_mov_b32_e32 v67, 0
	v_mov_b32_e32 v68, v206
	s_cbranch_vccz .LBB0_1052
	global_load_dwordx2 v[66:67], v[2:3], off

; template <int DQK, bool MOBA_OWN>
; __device__ __forceinline__ void attn_unit(LAS unsigned char* lds, int b, int h, int qb, const bf16_t* Qp, int ldq, const bf16_t* Kp, int ldk, const bf16_t* Vp, int ldv, bf16_t* Op, int ldo, const bf16_t* PO, const f32x2* PML) {
;     ...
; #pragma unroll
;         for (int sIdx = 0; sIdx < 3; ++sIdx) { ms[sIdx] = -1e30f; ws[sIdx] = 0.f; if (sIdx < nsel) { const f32x2 ml = PML[pidx + sIdx]; ms[sIdx] = ml[0]; ws[sIdx] = ml[1]; M = fmaxf(M, ml[0]); } }
.LBB0_1054:
	s_cmp_gt_u32 s8, 2
	s_cselect_b64 s[0:1], -1, 0
	s_cmp_lt_u32 s8, 3
	s_cbranch_scc1 .LBB0_1056
	global_load_dwordx2 v[44:45], v[2:3], off offset:16
	s_branch .LBB0_1057

; template <int DQK, bool MOBA_OWN>
; __device__ __forceinline__ void attn_unit(LAS unsigned char* lds, int b, int h, int qb, const bf16_t* Qp, int ldq, const bf16_t* Kp, int ldk, const bf16_t* Vp, int ldv, bf16_t* Op, int ldo, const bf16_t* PO, const f32x2* PML) {
;     ...
;         for (int sIdx = 0; sIdx < 3; ++sIdx) { ms[sIdx] = -1e30f; ws[sIdx] = 0.f; if (sIdx < nsel) { const f32x2 ml = PML[pidx + sIdx]; ms[sIdx] = ml[0]; ws[sIdx] = ml[1]; M = fmaxf(M, ml[0]); } }
;         const float w0 = __builtin_amdgcn_exp2f(m - M);
;         lt *= w0;
; #pragma unroll
;         for (int r = 0; r < 16; ++r) { o0[r] *= w0; o1[r] *= w0; }
; #pragma unroll
;         for (int sIdx = 0; sIdx < 3; ++sIdx) if (sIdx < nsel) {
;             const float w = ws[sIdx] * __builtin_amdgcn_exp2f(ms[sIdx] - M); lt += w;
;             const bf16_t* po = PO + (pidx + sIdx) * 64 + 4 * hi;
; #pragma unroll
;             for (int r4 = 0; r4 < 4; ++r4) { const u32x2 a = *(const u32x2*)(po + 8 * r4), c = *(const u32x2*)(po + 32 + 8 * r4);
;                 o0[4 * r4] += w * bflo(a.x); o0[4 * r4 + 1] += w * bfhi(a.x); o0[4 * r4 + 2] += w * bflo(a.y); o0[4 * r4 + 3] += w * bfhi(a.y);
;                 o1[4 * r4] += w * bflo(c.x); o1[4 * r4 + 1] += w * bfhi(c.x); o1[4 * r4 + 2] += w * bflo(c.y); o1[4 * r4 + 3] += w * bfhi(c.y); } }
.LBB0_1057:
	s_waitcnt vmcnt(0)
	v_max3_f32 v68, v206, v66, v48
	v_max_f32_e32 v68, v68, v44
	v_sub_f32_e32 v2, v206, v68
	v_exp_f32_e32 v70, v2
	s_andn2_b64 vcc, exec, s[6:7]
	v_readlane_b32 s6, v254, 8
	v_lshlrev_b32_e32 v178, 1, v201
	v_pk_mul_f32 v[38:39], v[20:21], v[70:71] op_sel_hi:[1,0]
	v_pk_mul_f32 v[20:21], v[24:25], v[70:71] op_sel_hi:[1,0]
	v_add_f32_e32 v24, v202, v69
	v_readlane_b32 s7, v254, 9
	v_pk_mul_f32 v[40:41], v[50:51], v[70:71] op_sel_hi:[1,0]
	v_pk_mul_f32 v[36:37], v[18:19], v[70:71] op_sel_hi:[1,0]
	v_pk_mul_f32 v[42:43], v[52:53], v[70:71] op_sel_hi:[1,0]
	v_pk_mul_f32 v[34:35], v[54:55], v[70:71] op_sel_hi:[1,0]
	v_pk_mul_f32 v[18:19], v[22:23], v[70:71] op_sel_hi:[1,0]
	v_pk_mul_f32 v[22:23], v[56:57], v[70:71] op_sel_hi:[1,0]
	v_pk_mul_f32 v[14:15], v[58:59], v[70:71] op_sel_hi:[1,0]
	v_pk_mul_f32 v[10:11], v[26:27], v[70:71] op_sel_hi:[1,0]
	v_pk_mul_f32 v[16:17], v[60:61], v[70:71] op_sel_hi:[1,0]
	v_pk_mul_f32 v[12:13], v[28:29], v[70:71] op_sel_hi:[1,0]
	v_pk_mul_f32 v[6:7], v[62:63], v[70:71] op_sel_hi:[1,0]
	v_pk_mul_f32 v[2:3], v[30:31], v[70:71] op_sel_hi:[1,0]
	v_pk_mul_f32 v[8:9], v[64:65], v[70:71] op_sel_hi:[1,0]
	v_pk_mul_f32 v[4:5], v[32:33], v[70:71] op_sel_hi:[1,0]
	v_mul_f32_e32 v27, v24, v70
	v_lshl_add_u64 v[24:25], s[6:7], 0, v[178:179]
	s_cbranch_vccnz .LBB0_1059
	s_movk_i32 s8, 0x180
	v_mad_u64_u32 v[28:29], s[6:7], v46, s8, v[24:25]
	v_mov_b32_e32 v30, v29
	v_mad_u64_u32 v[30:31], s[6:7], v47, s8, v[30:31]
	v_mov_b32_e32 v29, v30
	v_mov_b64_e32 v[30:31], v[72:73]
	v_mov_b64_e32 v[32:33], v[74:75]
	v_sub_f32_e32 v26, v66, v68
	v_exp_f32_e32 v52, v26
	s_waitcnt vmcnt(0)
	v_lshlrev_b32_e32 v50, 16, v30
	v_mul_f32_e32 v26, v67, v52
	v_and_b32_e32 v51, 0xffff0000, v30
	v_lshlrev_b32_e32 v30, 16, v31
	v_and_b32_e32 v31, 0xffff0000, v31
	v_pk_fma_f32 v[42:43], v[26:27], v[30:31], v[42:43] op_sel_hi:[0,1,1]
	v_lshlrev_b32_e32 v30, 16, v32
	v_and_b32_e32 v31, 0xffff0000, v32
	v_pk_fma_f32 v[36:37], v[26:27], v[30:31], v[36:37] op_sel_hi:[0,1,1]
	v_lshlrev_b32_e32 v30, 16, v33
	v_and_b32_e32 v31, 0xffff0000, v33
	v_pk_fma_f32 v[38:39], v[26:27], v[30:31], v[38:39] op_sel_hi:[0,1,1]
	v_mov_b64_e32 v[30:31], v[76:77]
	v_mov_b64_e32 v[32:33], v[78:79]
	v_pk_fma_f32 v[40:41], v[26:27], v[50:51], v[40:41] op_sel_hi:[0,1,1]
	s_waitcnt vmcnt(0)
	v_lshlrev_b32_e32 v50, 16, v30
	v_and_b32_e32 v51, 0xffff0000, v30
	v_lshlrev_b32_e32 v30, 16, v31
	v_and_b32_e32 v31, 0xffff0000, v31
	v_pk_fma_f32 v[22:23], v[26:27], v[30:31], v[22:23] op_sel_hi:[0,1,1]
	v_lshlrev_b32_e32 v30, 16, v32
	v_and_b32_e32 v31, 0xffff0000, v32
	v_pk_fma_f32 v[18:19], v[26:27], v[30:31], v[18:19] op_sel_hi:[0,1,1]
	v_lshlrev_b32_e32 v30, 16, v33
	v_and_b32_e32 v31, 0xffff0000, v33
	v_pk_fma_f32 v[20:21], v[26:27], v[30:31], v[20:21] op_sel_hi:[0,1,1]
	v_mov_b64_e32 v[30:31], v[80:81]
	v_mov_b64_e32 v[32:33], v[82:83]
	v_pk_fma_f32 v[34:35], v[26:27], v[50:51], v[34:35] op_sel_hi:[0,1,1]
	s_waitcnt vmcnt(0)
	v_lshlrev_b32_e32 v50, 16, v30
	v_and_b32_e32 v51, 0xffff0000, v30
	v_lshlrev_b32_e32 v30, 16, v31
	v_and_b32_e32 v31, 0xffff0000, v31
	v_pk_fma_f32 v[16:17], v[26:27], v[30:31], v[16:17] op_sel_hi:[0,1,1]
	v_lshlrev_b32_e32 v30, 16, v32
	v_and_b32_e32 v31, 0xffff0000, v32
	v_pk_fma_f32 v[10:11], v[26:27], v[30:31], v[10:11] op_sel_hi:[0,1,1]
	v_lshlrev_b32_e32 v30, 16, v33
	v_and_b32_e32 v31, 0xffff0000, v33
	v_pk_fma_f32 v[12:13], v[26:27], v[30:31], v[12:13] op_sel_hi:[0,1,1]
	v_mov_b64_e32 v[30:31], v[84:85]
	s_nop 0
	v_mov_b64_e32 v[28:29], v[86:87]
	v_pk_fma_f32 v[14:15], v[26:27], v[50:51], v[14:15] op_sel_hi:[0,1,1]
	s_waitcnt vmcnt(0)
	v_lshlrev_b32_e32 v32, 16, v30
	v_and_b32_e32 v33, 0xffff0000, v30
	v_lshlrev_b32_e32 v30, 16, v31
	v_and_b32_e32 v31, 0xffff0000, v31
	v_pk_fma_f32 v[8:9], v[26:27], v[30:31], v[8:9] op_sel_hi:[0,1,1]
	v_lshlrev_b32_e32 v30, 16, v28
	v_and_b32_e32 v31, 0xffff0000, v28
	v_lshlrev_b32_e32 v28, 16, v29
	v_and_b32_e32 v29, 0xffff0000, v29
	v_pk_fma_f32 v[6:7], v[26:27], v[32:33], v[6:7] op_sel_hi:[0,1,1]
	v_pk_fma_f32 v[2:3], v[26:27], v[30:31], v[2:3] op_sel_hi:[0,1,1]
	v_pk_fma_f32 v[4:5], v[26:27], v[28:29], v[4:5] op_sel_hi:[0,1,1]
	v_fmac_f32_e32 v27, v67, v52
; template <int DQK, bool MOBA_OWN>
; __device__ __forceinline__ void attn_unit(LAS unsigned char* lds, int b, int h, int qb, const bf16_t* Qp, int ldq, const bf16_t* Kp, int ldk, const bf16_t* Vp, int ldv, bf16_t* Op, int ldo, const bf16_t* PO, const f32x2* PML) {
;     ...
;         for (int sIdx = 0; sIdx < 3; ++sIdx) if (sIdx < nsel) {
;             const float w = ws[sIdx] * __builtin_amdgcn_exp2f(ms[sIdx] - M); lt += w;
;             const bf16_t* po = PO + (pidx + sIdx) * 64 + 4 * hi;
; #pragma unroll
;             for (int r4 = 0; r4 < 4; ++r4) { const u32x2 a = *(const u32x2*)(po + 8 * r4), c = *(const u32x2*)(po + 32 + 8 * r4);
;                 o0[4 * r4] += w * bflo(a.x); o0[4 * r4 + 1] += w * bfhi(a.x); o0[4 * r4 + 2] += w * bflo(a.y); o0[4 * r4 + 3] += w * bfhi(a.y);
;                 o1[4 * r4] += w * bflo(c.x); o1[4 * r4 + 1] += w * bfhi(c.x); o1[4 * r4 + 2] += w * bflo(c.y); o1[4 * r4 + 3] += w * bfhi(c.y); } }
.LBB0_1059:
	s_andn2_b64 vcc, exec, s[4:5]
	s_cbranch_vccnz .LBB0_1061
	s_movk_i32 s6, 0x180
	v_mad_u64_u32 v[28:29], s[4:5], v46, s6, v[24:25]
	v_mov_b32_e32 v30, v29
	v_mad_u64_u32 v[30:31], s[4:5], v47, s6, v[30:31]
	v_mov_b32_e32 v29, v30
	v_mov_b64_e32 v[30:31], v[88:89]
	v_mov_b64_e32 v[32:33], v[90:91]
	v_sub_f32_e32 v26, v48, v68
	v_exp_f32_e32 v48, v26
	s_waitcnt vmcnt(0)
	v_lshlrev_b32_e32 v50, 16, v30
	v_mul_f32_e32 v26, v49, v48
	v_and_b32_e32 v51, 0xffff0000, v30
	v_lshlrev_b32_e32 v30, 16, v31
	v_and_b32_e32 v31, 0xffff0000, v31
	v_pk_fma_f32 v[42:43], v[26:27], v[30:31], v[42:43] op_sel_hi:[0,1,1]
	v_lshlrev_b32_e32 v30, 16, v32
	v_and_b32_e32 v31, 0xffff0000, v32
	v_pk_fma_f32 v[36:37], v[26:27], v[30:31], v[36:37] op_sel_hi:[0,1,1]
	v_lshlrev_b32_e32 v30, 16, v33
	v_and_b32_e32 v31, 0xffff0000, v33
	v_pk_fma_f32 v[38:39], v[26:27], v[30:31], v[38:39] op_sel_hi:[0,1,1]
	v_mov_b64_e32 v[30:31], v[92:93]
	v_mov_b64_e32 v[32:33], v[94:95]
	v_pk_fma_f32 v[40:41], v[26:27], v[50:51], v[40:41] op_sel_hi:[0,1,1]
	s_waitcnt vmcnt(0)
	v_lshlrev_b32_e32 v50, 16, v30
	v_and_b32_e32 v51, 0xffff0000, v30
	v_lshlrev_b32_e32 v30, 16, v31
	v_and_b32_e32 v31, 0xffff0000, v31
	v_pk_fma_f32 v[22:23], v[26:27], v[30:31], v[22:23] op_sel_hi:[0,1,1]
	v_lshlrev_b32_e32 v30, 16, v32
	v_and_b32_e32 v31, 0xffff0000, v32
	v_pk_fma_f32 v[18:19], v[26:27], v[30:31], v[18:19] op_sel_hi:[0,1,1]
	v_lshlrev_b32_e32 v30, 16, v33
	v_and_b32_e32 v31, 0xffff0000, v33
	v_pk_fma_f32 v[20:21], v[26:27], v[30:31], v[20:21] op_sel_hi:[0,1,1]
	v_mov_b64_e32 v[30:31], v[96:97]
	v_mov_b64_e32 v[32:33], v[98:99]
	v_pk_fma_f32 v[34:35], v[26:27], v[50:51], v[34:35] op_sel_hi:[0,1,1]
	s_waitcnt vmcnt(0)
	v_lshlrev_b32_e32 v50, 16, v30
	v_and_b32_e32 v51, 0xffff0000, v30
	v_lshlrev_b32_e32 v30, 16, v31
	v_and_b32_e32 v31, 0xffff0000, v31
	v_pk_fma_f32 v[16:17], v[26:27], v[30:31], v[16:17] op_sel_hi:[0,1,1]
	v_lshlrev_b32_e32 v30, 16, v32
	v_and_b32_e32 v31, 0xffff0000, v32
	v_pk_fma_f32 v[10:11], v[26:27], v[30:31], v[10:11] op_sel_hi:[0,1,1]
	v_lshlrev_b32_e32 v30, 16, v33
	v_and_b32_e32 v31, 0xffff0000, v33
	v_pk_fma_f32 v[12:13], v[26:27], v[30:31], v[12:13] op_sel_hi:[0,1,1]
	v_mov_b64_e32 v[30:31], v[100:101]
	s_nop 0
	v_mov_b64_e32 v[28:29], v[102:103]
	v_pk_fma_f32 v[14:15], v[26:27], v[50:51], v[14:15] op_sel_hi:[0,1,1]
	s_waitcnt vmcnt(0)
	v_lshlrev_b32_e32 v32, 16, v30
	v_and_b32_e32 v33, 0xffff0000, v30
	v_lshlrev_b32_e32 v30, 16, v31
	v_and_b32_e32 v31, 0xffff0000, v31
	v_pk_fma_f32 v[8:9], v[26:27], v[30:31], v[8:9] op_sel_hi:[0,1,1]
	v_lshlrev_b32_e32 v30, 16, v28
	v_and_b32_e32 v31, 0xffff0000, v28
	v_lshlrev_b32_e32 v28, 16, v29
	v_and_b32_e32 v29, 0xffff0000, v29
	v_pk_fma_f32 v[6:7], v[26:27], v[32:33], v[6:7] op_sel_hi:[0,1,1]
	v_pk_fma_f32 v[2:3], v[26:27], v[30:31], v[2:3] op_sel_hi:[0,1,1]
	v_pk_fma_f32 v[4:5], v[26:27], v[28:29], v[4:5] op_sel_hi:[0,1,1]
	v_fmac_f32_e32 v27, v49, v48
.LBB0_1061:
	s_andn2_b64 vcc, exec, s[0:1]
	s_cbranch_vccnz .LBB0_999
	s_movk_i32 s4, 0x180
	v_mad_u64_u32 v[24:25], s[0:1], v46, s4, v[24:25]
	v_mov_b32_e32 v28, v25
	v_mad_u64_u32 v[28:29], s[0:1], v47, s4, v[28:29]
	v_mov_b32_e32 v25, v28
	v_mov_b64_e32 v[28:29], v[104:105]
	v_mov_b64_e32 v[30:31], v[106:107]
	v_sub_f32_e32 v26, v44, v68
	v_exp_f32_e32 v44, v26
	s_waitcnt vmcnt(0)
	v_lshlrev_b32_e32 v32, 16, v28
	v_mul_f32_e32 v26, v45, v44
	v_and_b32_e32 v33, 0xffff0000, v28
	v_lshlrev_b32_e32 v28, 16, v29
	v_and_b32_e32 v29, 0xffff0000, v29
	v_pk_fma_f32 v[42:43], v[26:27], v[28:29], v[42:43] op_sel_hi:[0,1,1]
	v_lshlrev_b32_e32 v28, 16, v30
	v_and_b32_e32 v29, 0xffff0000, v30
	v_pk_fma_f32 v[36:37], v[26:27], v[28:29], v[36:37] op_sel_hi:[0,1,1]
	v_lshlrev_b32_e32 v28, 16, v31
	v_and_b32_e32 v29, 0xffff0000, v31
	v_pk_fma_f32 v[38:39], v[26:27], v[28:29], v[38:39] op_sel_hi:[0,1,1]
	v_mov_b64_e32 v[28:29], v[108:109]
	v_mov_b64_e32 v[30:31], v[110:111]
	v_pk_fma_f32 v[40:41], v[26:27], v[32:33], v[40:41] op_sel_hi:[0,1,1]
	s_waitcnt vmcnt(0)
	v_lshlrev_b32_e32 v32, 16, v28
	v_and_b32_e32 v33, 0xffff0000, v28
	v_lshlrev_b32_e32 v28, 16, v29
	v_and_b32_e32 v29, 0xffff0000, v29
	v_pk_fma_f32 v[22:23], v[26:27], v[28:29], v[22:23] op_sel_hi:[0,1,1]
	v_lshlrev_b32_e32 v28, 16, v30
	v_and_b32_e32 v29, 0xffff0000, v30
	v_pk_fma_f32 v[18:19], v[26:27], v[28:29], v[18:19] op_sel_hi:[0,1,1]
	v_lshlrev_b32_e32 v28, 16, v31
	v_and_b32_e32 v29, 0xffff0000, v31
	v_pk_fma_f32 v[20:21], v[26:27], v[28:29], v[20:21] op_sel_hi:[0,1,1]
	v_mov_b64_e32 v[28:29], v[112:113]
	v_mov_b64_e32 v[30:31], v[114:115]
	v_pk_fma_f32 v[34:35], v[26:27], v[32:33], v[34:35] op_sel_hi:[0,1,1]
	s_waitcnt vmcnt(0)
	v_lshlrev_b32_e32 v32, 16, v28
	v_and_b32_e32 v33, 0xffff0000, v28
	v_lshlrev_b32_e32 v28, 16, v29
	v_and_b32_e32 v29, 0xffff0000, v29
	v_pk_fma_f32 v[16:17], v[26:27], v[28:29], v[16:17] op_sel_hi:[0,1,1]
	v_lshlrev_b32_e32 v28, 16, v30
	v_and_b32_e32 v29, 0xffff0000, v30
	v_pk_fma_f32 v[10:11], v[26:27], v[28:29], v[10:11] op_sel_hi:[0,1,1]
	v_lshlrev_b32_e32 v28, 16, v31
	v_and_b32_e32 v29, 0xffff0000, v31
	v_pk_fma_f32 v[12:13], v[26:27], v[28:29], v[12:13] op_sel_hi:[0,1,1]
	v_mov_b64_e32 v[28:29], v[116:117]
	s_nop 0
	v_mov_b64_e32 v[24:25], v[118:119]
	v_pk_fma_f32 v[14:15], v[26:27], v[32:33], v[14:15] op_sel_hi:[0,1,1]
	s_waitcnt vmcnt(0)
	v_lshlrev_b32_e32 v30, 16, v28
	v_and_b32_e32 v31, 0xffff0000, v28
	v_lshlrev_b32_e32 v28, 16, v29
	v_and_b32_e32 v29, 0xffff0000, v29
	v_pk_fma_f32 v[8:9], v[26:27], v[28:29], v[8:9] op_sel_hi:[0,1,1]
	v_lshlrev_b32_e32 v28, 16, v24
	v_and_b32_e32 v29, 0xffff0000, v24
	v_lshlrev_b32_e32 v24, 16, v25
	v_and_b32_e32 v25, 0xffff0000, v25
	v_pk_fma_f32 v[6:7], v[26:27], v[30:31], v[6:7] op_sel_hi:[0,1,1]
	v_pk_fma_f32 v[2:3], v[26:27], v[28:29], v[2:3] op_sel_hi:[0,1,1]
	v_pk_fma_f32 v[4:5], v[26:27], v[24:25], v[4:5] op_sel_hi:[0,1,1]
	v_fmac_f32_e32 v27, v45, v44
	s_branch .LBB0_999

; __device__ __forceinline__ float xhalf_sum(float v) { auto rr = __builtin_amdgcn_permlane32_swap(__float_as_uint(v), __float_as_uint(v), false, false); return __uint_as_float(rr[0]) + __uint_as_float(rr[1]); }
; template <int DQK, bool MOBA_OWN>
; __device__ __forceinline__ void attn_unit(LAS unsigned char* lds, int b, int h, int qb, const bf16_t* Qp, int ldq, const bf16_t* Kp, int ldk, const bf16_t* Vp, int ldv, bf16_t* Op, int ldo, const bf16_t* PO, const f32x2* PML) {
;     ...
;     float lt = xhalf_sum(l);
;     if (MOBA_OWN) {
;         const int nsel = qb < 3 ? qb : 3;
;         const size_t pidx = ((rowbase + tq) * 8 + h) * 3;
;         float ms[3], ws[3], M = m;
; #pragma unroll
;         for (int sIdx = 0; sIdx < 3; ++sIdx) { ms[sIdx] = -1e30f; ws[sIdx] = 0.f; if (sIdx < nsel) { const f32x2 ml = PML[pidx + sIdx]; ms[sIdx] = ml[0]; ws[sIdx] = ml[1]; M = fmaxf(M, ml[0]); } }
.LBB0_3509:
	v_lshlrev_b64 v[46:47], 3, v[184:185]
	v_or_b32_e32 v46, s73, v46
	v_readlane_b32 s0, v254, 10
	v_readlane_b32 s73, v255, 7
	v_readlane_b32 s1, v254, 11
	s_cmp_lg_u32 s73, 0
	v_mov_b32_e32 v69, v202
	v_mad_u64_u32 v[2:3], s[0:1], v46, 24, s[0:1]
	s_cselect_b64 s[4:5], -1, 0
	v_permlane32_swap_b32_e32 v202, v69
	v_mad_i32_i24 v3, v47, 24, v3
	v_readlane_b32 s0, v254, 8
	v_readlane_b32 s1, v254, 9
	v_lshlrev_b32_e32 v126, 1, v201
	v_mov_b32_e32 v127, 0
	s_nop 0
	v_lshl_add_u64 v[126:127], s[0:1], 0, v[126:127]
	s_movk_i32 s0, 0x180
	v_mad_u64_u32 v[126:127], vcc, v46, s0, v[126:127]
	v_mov_b32_e32 v128, v127
	v_mad_u64_u32 v[128:129], vcc, v47, s0, v[128:129]
	v_mov_b32_e32 v127, v128
	global_load_dwordx2 v[72:73], v[126:127], off
	global_load_dwordx2 v[74:75], v[126:127], off offset:64
	global_load_dwordx2 v[76:77], v[126:127], off offset:16
	global_load_dwordx2 v[78:79], v[126:127], off offset:80
	global_load_dwordx2 v[80:81], v[126:127], off offset:32
	global_load_dwordx2 v[82:83], v[126:127], off offset:96
	global_load_dwordx2 v[84:85], v[126:127], off offset:48
	global_load_dwordx2 v[86:87], v[126:127], off offset:112
	global_load_dwordx2 v[88:89], v[126:127], off offset:128
	global_load_dwordx2 v[90:91], v[126:127], off offset:192
	global_load_dwordx2 v[92:93], v[126:127], off offset:144
	global_load_dwordx2 v[94:95], v[126:127], off offset:208
	global_load_dwordx2 v[96:97], v[126:127], off offset:160
	global_load_dwordx2 v[98:99], v[126:127], off offset:224
	global_load_dwordx2 v[100:101], v[126:127], off offset:176
	global_load_dwordx2 v[102:103], v[126:127], off offset:240
	global_load_dwordx2 v[104:105], v[126:127], off offset:256
	global_load_dwordx2 v[106:107], v[126:127], off offset:320
	global_load_dwordx2 v[108:109], v[126:127], off offset:272
	global_load_dwordx2 v[110:111], v[126:127], off offset:336
	global_load_dwordx2 v[112:113], v[126:127], off offset:288
	global_load_dwordx2 v[114:115], v[126:127], off offset:352
	global_load_dwordx2 v[116:117], v[126:127], off offset:304
	global_load_dwordx2 v[118:119], v[126:127], off offset:368
	v_mov_b32_e32 v49, 0
	v_mov_b32_e32 v48, 0xf149f2ca
	s_and_b64 vcc, exec, s[4:5]
	v_mov_b32_e32 v66, 0xf149f2ca
	v_mov_b32_e32 v67, 0
	v_mov_b32_e32 v68, v206
	s_cbranch_vccz .LBB0_3511
	global_load_dwordx2 v[66:67], v[2:3], off

; template <int DQK, bool MOBA_OWN>
; __device__ __forceinline__ void attn_unit(LAS unsigned char* lds, int b, int h, int qb, const bf16_t* Qp, int ldq, const bf16_t* Kp, int ldk, const bf16_t* Vp, int ldv, bf16_t* Op, int ldo, const bf16_t* PO, const f32x2* PML) {
;     ...
; #pragma unroll
;         for (int sIdx = 0; sIdx < 3; ++sIdx) { ms[sIdx] = -1e30f; ws[sIdx] = 0.f; if (sIdx < nsel) { const f32x2 ml = PML[pidx + sIdx]; ms[sIdx] = ml[0]; ws[sIdx] = ml[1]; M = fmaxf(M, ml[0]); } }
.LBB0_3513:
	s_cmp_gt_u32 s73, 2
	s_cselect_b64 s[0:1], -1, 0
	s_cmp_lt_u32 s73, 3
	s_cbranch_scc1 .LBB0_3515
	global_load_dwordx2 v[44:45], v[2:3], off offset:16
	s_branch .LBB0_3516

; template <int DQK, bool MOBA_OWN>
; __device__ __forceinline__ void attn_unit(LAS unsigned char* lds, int b, int h, int qb, const bf16_t* Qp, int ldq, const bf16_t* Kp, int ldk, const bf16_t* Vp, int ldv, bf16_t* Op, int ldo, const bf16_t* PO, const f32x2* PML) {
;     ...
;         for (int sIdx = 0; sIdx < 3; ++sIdx) { ms[sIdx] = -1e30f; ws[sIdx] = 0.f; if (sIdx < nsel) { const f32x2 ml = PML[pidx + sIdx]; ms[sIdx] = ml[0]; ws[sIdx] = ml[1]; M = fmaxf(M, ml[0]); } }
;         const float w0 = __builtin_amdgcn_exp2f(m - M);
;         lt *= w0;
; #pragma unroll
;         for (int r = 0; r < 16; ++r) { o0[r] *= w0; o1[r] *= w0; }
; #pragma unroll
;         for (int sIdx = 0; sIdx < 3; ++sIdx) if (sIdx < nsel) {
;             const float w = ws[sIdx] * __builtin_amdgcn_exp2f(ms[sIdx] - M); lt += w;
;             const bf16_t* po = PO + (pidx + sIdx) * 64 + 4 * hi;
; #pragma unroll
;             for (int r4 = 0; r4 < 4; ++r4) { const u32x2 a = *(const u32x2*)(po + 8 * r4), c = *(const u32x2*)(po + 32 + 8 * r4);
;                 o0[4 * r4] += w * bflo(a.x); o0[4 * r4 + 1] += w * bfhi(a.x); o0[4 * r4 + 2] += w * bflo(a.y); o0[4 * r4 + 3] += w * bfhi(a.y);
;                 o1[4 * r4] += w * bflo(c.x); o1[4 * r4 + 1] += w * bfhi(c.x); o1[4 * r4 + 2] += w * bflo(c.y); o1[4 * r4 + 3] += w * bfhi(c.y); } }
.LBB0_3516:
	s_waitcnt vmcnt(0)
	v_max3_f32 v68, v206, v66, v48
	v_max_f32_e32 v68, v68, v44
	v_sub_f32_e32 v2, v206, v68
	v_exp_f32_e32 v70, v2
	s_andn2_b64 vcc, exec, s[4:5]
	v_readlane_b32 s4, v254, 8
	v_lshlrev_b32_e32 v178, 1, v201
	v_pk_mul_f32 v[38:39], v[20:21], v[70:71] op_sel_hi:[1,0]
	v_pk_mul_f32 v[20:21], v[24:25], v[70:71] op_sel_hi:[1,0]
	v_add_f32_e32 v24, v202, v69
	v_readlane_b32 s5, v254, 9
	v_pk_mul_f32 v[40:41], v[50:51], v[70:71] op_sel_hi:[1,0]
	v_pk_mul_f32 v[36:37], v[18:19], v[70:71] op_sel_hi:[1,0]
	v_pk_mul_f32 v[42:43], v[52:53], v[70:71] op_sel_hi:[1,0]
	v_pk_mul_f32 v[34:35], v[54:55], v[70:71] op_sel_hi:[1,0]
	v_pk_mul_f32 v[18:19], v[22:23], v[70:71] op_sel_hi:[1,0]
	v_pk_mul_f32 v[22:23], v[56:57], v[70:71] op_sel_hi:[1,0]
	v_pk_mul_f32 v[14:15], v[58:59], v[70:71] op_sel_hi:[1,0]
	v_pk_mul_f32 v[10:11], v[26:27], v[70:71] op_sel_hi:[1,0]
	v_pk_mul_f32 v[16:17], v[60:61], v[70:71] op_sel_hi:[1,0]
	v_pk_mul_f32 v[12:13], v[28:29], v[70:71] op_sel_hi:[1,0]
	v_pk_mul_f32 v[6:7], v[62:63], v[70:71] op_sel_hi:[1,0]
	v_pk_mul_f32 v[2:3], v[30:31], v[70:71] op_sel_hi:[1,0]
	v_pk_mul_f32 v[8:9], v[64:65], v[70:71] op_sel_hi:[1,0]
	v_pk_mul_f32 v[4:5], v[32:33], v[70:71] op_sel_hi:[1,0]
	v_mul_f32_e32 v27, v24, v70
	v_lshl_add_u64 v[24:25], s[4:5], 0, v[178:179]
	s_cbranch_vccnz .LBB0_3518
	s_movk_i32 s6, 0x180
	v_mad_u64_u32 v[28:29], s[4:5], v46, s6, v[24:25]
	v_mov_b32_e32 v30, v29
	v_mad_u64_u32 v[30:31], s[4:5], v47, s6, v[30:31]
	v_mov_b32_e32 v29, v30
	v_mov_b64_e32 v[30:31], v[72:73]
	v_mov_b64_e32 v[32:33], v[74:75]
	v_sub_f32_e32 v26, v66, v68
	v_exp_f32_e32 v52, v26
	s_waitcnt vmcnt(0)
	v_lshlrev_b32_e32 v50, 16, v30
	v_mul_f32_e32 v26, v67, v52
	v_and_b32_e32 v51, 0xffff0000, v30
	v_lshlrev_b32_e32 v30, 16, v31
	v_and_b32_e32 v31, 0xffff0000, v31
	v_pk_fma_f32 v[42:43], v[26:27], v[30:31], v[42:43] op_sel_hi:[0,1,1]
	v_lshlrev_b32_e32 v30, 16, v32
	v_and_b32_e32 v31, 0xffff0000, v32
	v_pk_fma_f32 v[36:37], v[26:27], v[30:31], v[36:37] op_sel_hi:[0,1,1]
	v_lshlrev_b32_e32 v30, 16, v33
	v_and_b32_e32 v31, 0xffff0000, v33
	v_pk_fma_f32 v[38:39], v[26:27], v[30:31], v[38:39] op_sel_hi:[0,1,1]
	v_mov_b64_e32 v[30:31], v[76:77]
	v_mov_b64_e32 v[32:33], v[78:79]
	v_pk_fma_f32 v[40:41], v[26:27], v[50:51], v[40:41] op_sel_hi:[0,1,1]
	s_waitcnt vmcnt(0)
	v_lshlrev_b32_e32 v50, 16, v30
	v_and_b32_e32 v51, 0xffff0000, v30
	v_lshlrev_b32_e32 v30, 16, v31
	v_and_b32_e32 v31, 0xffff0000, v31
	v_pk_fma_f32 v[22:23], v[26:27], v[30:31], v[22:23] op_sel_hi:[0,1,1]
	v_lshlrev_b32_e32 v30, 16, v32
	v_and_b32_e32 v31, 0xffff0000, v32
	v_pk_fma_f32 v[18:19], v[26:27], v[30:31], v[18:19] op_sel_hi:[0,1,1]
	v_lshlrev_b32_e32 v30, 16, v33
	v_and_b32_e32 v31, 0xffff0000, v33
	v_pk_fma_f32 v[20:21], v[26:27], v[30:31], v[20:21] op_sel_hi:[0,1,1]
	v_mov_b64_e32 v[30:31], v[80:81]
	v_mov_b64_e32 v[32:33], v[82:83]
	v_pk_fma_f32 v[34:35], v[26:27], v[50:51], v[34:35] op_sel_hi:[0,1,1]
	s_waitcnt vmcnt(0)
	v_lshlrev_b32_e32 v50, 16, v30
	v_and_b32_e32 v51, 0xffff0000, v30
	v_lshlrev_b32_e32 v30, 16, v31
	v_and_b32_e32 v31, 0xffff0000, v31
	v_pk_fma_f32 v[16:17], v[26:27], v[30:31], v[16:17] op_sel_hi:[0,1,1]
	v_lshlrev_b32_e32 v30, 16, v32
	v_and_b32_e32 v31, 0xffff0000, v32
	v_pk_fma_f32 v[10:11], v[26:27], v[30:31], v[10:11] op_sel_hi:[0,1,1]
	v_lshlrev_b32_e32 v30, 16, v33
	v_and_b32_e32 v31, 0xffff0000, v33
	v_pk_fma_f32 v[12:13], v[26:27], v[30:31], v[12:13] op_sel_hi:[0,1,1]
	v_mov_b64_e32 v[30:31], v[84:85]
	s_nop 0
	v_mov_b64_e32 v[28:29], v[86:87]
	v_pk_fma_f32 v[14:15], v[26:27], v[50:51], v[14:15] op_sel_hi:[0,1,1]
	s_waitcnt vmcnt(0)
	v_lshlrev_b32_e32 v32, 16, v30
	v_and_b32_e32 v33, 0xffff0000, v30
	v_lshlrev_b32_e32 v30, 16, v31
	v_and_b32_e32 v31, 0xffff0000, v31
	v_pk_fma_f32 v[8:9], v[26:27], v[30:31], v[8:9] op_sel_hi:[0,1,1]
	v_lshlrev_b32_e32 v30, 16, v28
	v_and_b32_e32 v31, 0xffff0000, v28
	v_lshlrev_b32_e32 v28, 16, v29
	v_and_b32_e32 v29, 0xffff0000, v29
	v_pk_fma_f32 v[6:7], v[26:27], v[32:33], v[6:7] op_sel_hi:[0,1,1]
	v_pk_fma_f32 v[2:3], v[26:27], v[30:31], v[2:3] op_sel_hi:[0,1,1]
	v_pk_fma_f32 v[4:5], v[26:27], v[28:29], v[4:5] op_sel_hi:[0,1,1]
	v_fmac_f32_e32 v27, v67, v52
; template <int DQK, bool MOBA_OWN>
; __device__ __forceinline__ void attn_unit(LAS unsigned char* lds, int b, int h, int qb, const bf16_t* Qp, int ldq, const bf16_t* Kp, int ldk, const bf16_t* Vp, int ldv, bf16_t* Op, int ldo, const bf16_t* PO, const f32x2* PML) {
;     ...
;         for (int sIdx = 0; sIdx < 3; ++sIdx) if (sIdx < nsel) {
;             const float w = ws[sIdx] * __builtin_amdgcn_exp2f(ms[sIdx] - M); lt += w;
;             const bf16_t* po = PO + (pidx + sIdx) * 64 + 4 * hi;
; #pragma unroll
;             for (int r4 = 0; r4 < 4; ++r4) { const u32x2 a = *(const u32x2*)(po + 8 * r4), c = *(const u32x2*)(po + 32 + 8 * r4);
;                 o0[4 * r4] += w * bflo(a.x); o0[4 * r4 + 1] += w * bfhi(a.x); o0[4 * r4 + 2] += w * bflo(a.y); o0[4 * r4 + 3] += w * bfhi(a.y);
;                 o1[4 * r4] += w * bflo(c.x); o1[4 * r4 + 1] += w * bfhi(c.x); o1[4 * r4 + 2] += w * bflo(c.y); o1[4 * r4 + 3] += w * bfhi(c.y); } }
.LBB0_3518:
	s_andn2_b64 vcc, exec, s[2:3]
	s_cbranch_vccnz .LBB0_3520
	s_movk_i32 s4, 0x180
	v_mad_u64_u32 v[28:29], s[2:3], v46, s4, v[24:25]
	v_mov_b32_e32 v30, v29
	v_mad_u64_u32 v[30:31], s[2:3], v47, s4, v[30:31]
	v_mov_b32_e32 v29, v30
	v_mov_b64_e32 v[30:31], v[88:89]
	v_mov_b64_e32 v[32:33], v[90:91]
	v_sub_f32_e32 v26, v48, v68
	v_exp_f32_e32 v48, v26
	s_waitcnt vmcnt(0)
	v_lshlrev_b32_e32 v50, 16, v30
	v_mul_f32_e32 v26, v49, v48
	v_and_b32_e32 v51, 0xffff0000, v30
	v_lshlrev_b32_e32 v30, 16, v31
	v_and_b32_e32 v31, 0xffff0000, v31
	v_pk_fma_f32 v[42:43], v[26:27], v[30:31], v[42:43] op_sel_hi:[0,1,1]
	v_lshlrev_b32_e32 v30, 16, v32
	v_and_b32_e32 v31, 0xffff0000, v32
	v_pk_fma_f32 v[36:37], v[26:27], v[30:31], v[36:37] op_sel_hi:[0,1,1]
	v_lshlrev_b32_e32 v30, 16, v33
	v_and_b32_e32 v31, 0xffff0000, v33
	v_pk_fma_f32 v[38:39], v[26:27], v[30:31], v[38:39] op_sel_hi:[0,1,1]
	v_mov_b64_e32 v[30:31], v[92:93]
	v_mov_b64_e32 v[32:33], v[94:95]
	v_pk_fma_f32 v[40:41], v[26:27], v[50:51], v[40:41] op_sel_hi:[0,1,1]
	s_waitcnt vmcnt(0)
	v_lshlrev_b32_e32 v50, 16, v30
	v_and_b32_e32 v51, 0xffff0000, v30
	v_lshlrev_b32_e32 v30, 16, v31
	v_and_b32_e32 v31, 0xffff0000, v31
	v_pk_fma_f32 v[22:23], v[26:27], v[30:31], v[22:23] op_sel_hi:[0,1,1]
	v_lshlrev_b32_e32 v30, 16, v32
	v_and_b32_e32 v31, 0xffff0000, v32
	v_pk_fma_f32 v[18:19], v[26:27], v[30:31], v[18:19] op_sel_hi:[0,1,1]
	v_lshlrev_b32_e32 v30, 16, v33
	v_and_b32_e32 v31, 0xffff0000, v33
	v_pk_fma_f32 v[20:21], v[26:27], v[30:31], v[20:21] op_sel_hi:[0,1,1]
	v_mov_b64_e32 v[30:31], v[96:97]
	v_mov_b64_e32 v[32:33], v[98:99]
	v_pk_fma_f32 v[34:35], v[26:27], v[50:51], v[34:35] op_sel_hi:[0,1,1]
	s_waitcnt vmcnt(0)
	v_lshlrev_b32_e32 v50, 16, v30
	v_and_b32_e32 v51, 0xffff0000, v30
	v_lshlrev_b32_e32 v30, 16, v31
	v_and_b32_e32 v31, 0xffff0000, v31
	v_pk_fma_f32 v[16:17], v[26:27], v[30:31], v[16:17] op_sel_hi:[0,1,1]
	v_lshlrev_b32_e32 v30, 16, v32
	v_and_b32_e32 v31, 0xffff0000, v32
	v_pk_fma_f32 v[10:11], v[26:27], v[30:31], v[10:11] op_sel_hi:[0,1,1]
	v_lshlrev_b32_e32 v30, 16, v33
	v_and_b32_e32 v31, 0xffff0000, v33
	v_pk_fma_f32 v[12:13], v[26:27], v[30:31], v[12:13] op_sel_hi:[0,1,1]
	v_mov_b64_e32 v[30:31], v[100:101]
	s_nop 0
	v_mov_b64_e32 v[28:29], v[102:103]
	v_pk_fma_f32 v[14:15], v[26:27], v[50:51], v[14:15] op_sel_hi:[0,1,1]
	s_waitcnt vmcnt(0)
	v_lshlrev_b32_e32 v32, 16, v30
	v_and_b32_e32 v33, 0xffff0000, v30
	v_lshlrev_b32_e32 v30, 16, v31
	v_and_b32_e32 v31, 0xffff0000, v31
	v_pk_fma_f32 v[8:9], v[26:27], v[30:31], v[8:9] op_sel_hi:[0,1,1]
	v_lshlrev_b32_e32 v30, 16, v28
	v_and_b32_e32 v31, 0xffff0000, v28
	v_lshlrev_b32_e32 v28, 16, v29
	v_and_b32_e32 v29, 0xffff0000, v29
	v_pk_fma_f32 v[6:7], v[26:27], v[32:33], v[6:7] op_sel_hi:[0,1,1]
	v_pk_fma_f32 v[2:3], v[26:27], v[30:31], v[2:3] op_sel_hi:[0,1,1]
	v_pk_fma_f32 v[4:5], v[26:27], v[28:29], v[4:5] op_sel_hi:[0,1,1]
	v_fmac_f32_e32 v27, v49, v48
.LBB0_3520:
	s_andn2_b64 vcc, exec, s[0:1]
	s_cbranch_vccnz .LBB0_3458
	s_movk_i32 s2, 0x180
	v_mad_u64_u32 v[24:25], s[0:1], v46, s2, v[24:25]
	v_mov_b32_e32 v28, v25
	v_mad_u64_u32 v[28:29], s[0:1], v47, s2, v[28:29]
	v_mov_b32_e32 v25, v28
	v_mov_b64_e32 v[28:29], v[104:105]
	v_mov_b64_e32 v[30:31], v[106:107]
	v_sub_f32_e32 v26, v44, v68
	v_exp_f32_e32 v44, v26
	s_waitcnt vmcnt(0)
	v_lshlrev_b32_e32 v32, 16, v28
	v_mul_f32_e32 v26, v45, v44
	v_and_b32_e32 v33, 0xffff0000, v28
	v_lshlrev_b32_e32 v28, 16, v29
	v_and_b32_e32 v29, 0xffff0000, v29
	v_pk_fma_f32 v[42:43], v[26:27], v[28:29], v[42:43] op_sel_hi:[0,1,1]
	v_lshlrev_b32_e32 v28, 16, v30
	v_and_b32_e32 v29, 0xffff0000, v30
	v_pk_fma_f32 v[36:37], v[26:27], v[28:29], v[36:37] op_sel_hi:[0,1,1]
	v_lshlrev_b32_e32 v28, 16, v31
	v_and_b32_e32 v29, 0xffff0000, v31
	v_pk_fma_f32 v[38:39], v[26:27], v[28:29], v[38:39] op_sel_hi:[0,1,1]
	v_mov_b64_e32 v[28:29], v[108:109]
	v_mov_b64_e32 v[30:31], v[110:111]
	v_pk_fma_f32 v[40:41], v[26:27], v[32:33], v[40:41] op_sel_hi:[0,1,1]
	s_waitcnt vmcnt(0)
	v_lshlrev_b32_e32 v32, 16, v28
	v_and_b32_e32 v33, 0xffff0000, v28
	v_lshlrev_b32_e32 v28, 16, v29
	v_and_b32_e32 v29, 0xffff0000, v29
	v_pk_fma_f32 v[22:23], v[26:27], v[28:29], v[22:23] op_sel_hi:[0,1,1]
	v_lshlrev_b32_e32 v28, 16, v30
	v_and_b32_e32 v29, 0xffff0000, v30
	v_pk_fma_f32 v[18:19], v[26:27], v[28:29], v[18:19] op_sel_hi:[0,1,1]
	v_lshlrev_b32_e32 v28, 16, v31
	v_and_b32_e32 v29, 0xffff0000, v31
	v_pk_fma_f32 v[20:21], v[26:27], v[28:29], v[20:21] op_sel_hi:[0,1,1]
	v_mov_b64_e32 v[28:29], v[112:113]
	v_mov_b64_e32 v[30:31], v[114:115]
	v_pk_fma_f32 v[34:35], v[26:27], v[32:33], v[34:35] op_sel_hi:[0,1,1]
	s_waitcnt vmcnt(0)
	v_lshlrev_b32_e32 v32, 16, v28
	v_and_b32_e32 v33, 0xffff0000, v28
	v_lshlrev_b32_e32 v28, 16, v29
	v_and_b32_e32 v29, 0xffff0000, v29
	v_pk_fma_f32 v[16:17], v[26:27], v[28:29], v[16:17] op_sel_hi:[0,1,1]
	v_lshlrev_b32_e32 v28, 16, v30
	v_and_b32_e32 v29, 0xffff0000, v30
	v_pk_fma_f32 v[10:11], v[26:27], v[28:29], v[10:11] op_sel_hi:[0,1,1]
	v_lshlrev_b32_e32 v28, 16, v31
	v_and_b32_e32 v29, 0xffff0000, v31
	v_pk_fma_f32 v[12:13], v[26:27], v[28:29], v[12:13] op_sel_hi:[0,1,1]
	v_mov_b64_e32 v[28:29], v[116:117]
	s_nop 0
	v_mov_b64_e32 v[24:25], v[118:119]
	v_pk_fma_f32 v[14:15], v[26:27], v[32:33], v[14:15] op_sel_hi:[0,1,1]
	s_waitcnt vmcnt(0)
	v_lshlrev_b32_e32 v30, 16, v28
	v_and_b32_e32 v31, 0xffff0000, v28
	v_lshlrev_b32_e32 v28, 16, v29
	v_and_b32_e32 v29, 0xffff0000, v29
	v_pk_fma_f32 v[8:9], v[26:27], v[28:29], v[8:9] op_sel_hi:[0,1,1]
	v_lshlrev_b32_e32 v28, 16, v24
	v_and_b32_e32 v29, 0xffff0000, v24
	v_lshlrev_b32_e32 v24, 16, v25
	v_and_b32_e32 v25, 0xffff0000, v25
	v_pk_fma_f32 v[6:7], v[26:27], v[30:31], v[6:7] op_sel_hi:[0,1,1]
	v_pk_fma_f32 v[2:3], v[26:27], v[28:29], v[2:3] op_sel_hi:[0,1,1]
	v_pk_fma_f32 v[4:5], v[26:27], v[24:25], v[4:5] op_sel_hi:[0,1,1]
	v_fmac_f32_e32 v27, v45, v44
	s_branch .LBB0_3458
